# v11 + one static s_setprio 1 for waves 4-7 during each attention unit (reset at the unit's closing barrier)
# speedup vs baseline: 1.0005x; 1.0005x over previous
.LBB0_871:
	s_or_b64 exec, exec, s[4:5]
	s_waitcnt lgkmcnt(0)
	ds_read_b128 v[6:9], v4 offset:49280
	ds_read_b128 v[10:13], v4 offset:49312
	s_cmp_eq_u32 s74, 0
	s_cselect_b32 s2, s91, 0x3ec00000
	s_add_u32 s4, s52, s2
	s_waitcnt lgkmcnt(1)
	v_rcp_f32_e32 v2, v6
	v_rcp_f32_e32 v5, v7
	v_rcp_f32_e32 v14, v8
	v_rcp_f32_e32 v15, v9
	s_waitcnt lgkmcnt(0)
	v_rcp_f32_e32 v16, v10
	ds_read_b128 v[6:9], v4 offset:49344
	v_rcp_f32_e32 v17, v11
	v_rcp_f32_e32 v50, v12
	v_rcp_f32_e32 v51, v13
	ds_read_b128 v[10:13], v4 offset:49376
	s_addc_u32 s5, s53, 0
	s_lshl_b64 s[2:3], s[6:7], 1
	s_add_u32 s2, s4, s2
	s_addc_u32 s3, s5, s3
	s_lshl_b32 s4, s19, 12
	s_waitcnt lgkmcnt(1)
	v_rcp_f32_e32 v4, v6
	v_rcp_f32_e32 v6, v7
	v_rcp_f32_e32 v7, v8
	v_rcp_f32_e32 v8, v9
	s_waitcnt lgkmcnt(0)
	v_rcp_f32_e32 v9, v10
	v_rcp_f32_e32 v10, v11
	v_rcp_f32_e32 v11, v12
	v_rcp_f32_e32 v12, v13
	s_add_i32 s4, s4, 0
	v_lshlrev_b32_e32 v13, 1, v226
	v_mul_f32_e32 v34, v34, v2
	v_mul_f32_e32 v2, v18, v2
	v_add3_u32 v13, s4, v232, v13
	v_cvt_pk_bf16_f32 v2, v2, s0
	ds_write_b16 v13, v2 offset:51264
	v_mul_f32_e32 v2, v35, v5
	v_cvt_pk_bf16_f32 v2, v2, s0
	ds_write_b16 v13, v2 offset:51328
	v_mul_f32_e32 v2, v19, v5
	v_cvt_pk_bf16_f32 v2, v2, s0
	ds_write_b16 v13, v2 offset:51392
	v_mul_f32_e32 v2, v36, v14
	v_cvt_pk_bf16_f32 v2, v2, s0
	ds_write_b16 v13, v2 offset:51456
	v_mul_f32_e32 v2, v20, v14
	v_cvt_pk_bf16_f32 v2, v2, s0
	ds_write_b16 v13, v2 offset:51520
	v_mul_f32_e32 v2, v37, v15
	v_cvt_pk_bf16_f32 v2, v2, s0
	ds_write_b16 v13, v2 offset:51584
	v_mul_f32_e32 v2, v21, v15
	v_cvt_pk_bf16_f32 v2, v2, s0
	ds_write_b16 v13, v2 offset:51648
	v_mul_f32_e32 v2, v38, v16
	v_cvt_pk_bf16_f32 v2, v2, s0
	ds_write_b16 v13, v2 offset:52224
	v_mul_f32_e32 v2, v22, v16
	v_cvt_pk_bf16_f32 v2, v2, s0
	ds_write_b16 v13, v2 offset:52288
	v_mul_f32_e32 v2, v39, v17
	v_cvt_pk_bf16_f32 v2, v2, s0
	ds_write_b16 v13, v2 offset:52352
	v_mul_f32_e32 v2, v23, v17
	v_cvt_pk_bf16_f32 v2, v2, s0
	ds_write_b16 v13, v2 offset:52416
	v_mul_f32_e32 v2, v40, v50
	v_cvt_pk_bf16_f32 v2, v2, s0
	ds_write_b16 v13, v2 offset:52480
	v_mul_f32_e32 v2, v24, v50
	v_cvt_pk_bf16_f32 v2, v2, s0
	ds_write_b16 v13, v2 offset:52544
	v_mul_f32_e32 v2, v41, v51
	v_cvt_pk_bf16_f32 v2, v2, s0
	ds_write_b16 v13, v2 offset:52608
	v_mul_f32_e32 v2, v25, v51
	v_cvt_pk_bf16_f32 v2, v2, s0
	ds_write_b16 v13, v2 offset:52672
	v_mul_f32_e32 v2, v42, v4
	v_cvt_pk_bf16_f32 v2, v2, s0
	ds_write_b16 v13, v2 offset:53248
	v_mul_f32_e32 v2, v26, v4
	v_cvt_pk_bf16_f32 v2, v2, s0
	ds_write_b16 v13, v2 offset:53312
	v_mul_f32_e32 v2, v43, v6
	v_cvt_pk_bf16_f32 v2, v2, s0
	ds_write_b16 v13, v2 offset:53376
	v_mul_f32_e32 v2, v27, v6
	v_cvt_pk_bf16_f32 v2, v2, s0
	ds_write_b16 v13, v2 offset:53440
	v_mul_f32_e32 v2, v44, v7
	v_cvt_pk_bf16_f32 v2, v2, s0
	ds_write_b16 v13, v2 offset:53504
	v_mul_f32_e32 v2, v28, v7
	v_cvt_pk_bf16_f32 v2, v2, s0
	ds_write_b16 v13, v2 offset:53568
	v_mul_f32_e32 v2, v45, v8
	v_cvt_pk_bf16_f32 v2, v2, s0
	ds_write_b16 v13, v2 offset:53632
	v_mul_f32_e32 v2, v29, v8
	v_cvt_pk_bf16_f32 v2, v2, s0
	ds_write_b16 v13, v2 offset:53696
	v_mul_f32_e32 v2, v46, v9
	v_cvt_pk_bf16_f32 v2, v2, s0
	ds_write_b16 v13, v2 offset:54272
	v_mul_f32_e32 v2, v30, v9
	v_cvt_pk_bf16_f32 v2, v2, s0
	ds_write_b16 v13, v2 offset:54336
	v_mul_f32_e32 v2, v47, v10
	v_cvt_pk_bf16_f32 v2, v2, s0
	ds_write_b16 v13, v2 offset:54400
	v_mul_f32_e32 v2, v31, v10
	v_cvt_pk_bf16_f32 v2, v2, s0
	ds_write_b16 v13, v2 offset:54464
	v_mul_f32_e32 v2, v48, v11
	v_cvt_pk_bf16_f32 v2, v2, s0
	ds_write_b16 v13, v2 offset:54528
	v_mul_f32_e32 v2, v32, v11
	v_cvt_pk_bf16_f32 v2, v2, s0
	ds_write_b16 v13, v2 offset:54592
	v_mul_f32_e32 v2, v49, v12
	v_cvt_pk_bf16_f32 v2, v2, s0
	ds_write_b16 v13, v2 offset:54656
	v_mul_f32_e32 v2, v33, v12
	v_cvt_pk_bf16_f32 v34, v34, s0
	v_cvt_pk_bf16_f32 v2, v2, s0
	ds_write_b16 v13, v34 offset:51200
	ds_write_b16 v13, v2 offset:54720
	v_add_u32_e32 v2, s4, v206
	s_waitcnt lgkmcnt(0)
	v_add_u32_e32 v4, v2, v233
	s_lshl_b32 s5, s33, 1
	ds_read_b128 v[4:7], v4 offset:51200
	v_add_u32_e32 v8, v2, v234
	s_add_u32 s2, s2, s5
	ds_read_b128 v[8:11], v8 offset:51200
	s_addc_u32 s3, s3, 0
	v_mov_b32_e32 v207, v3
	v_lshl_add_u64 v[12:13], s[2:3], 0, v[206:207]
	v_mov_b32_e32 v209, v3
	v_lshl_add_u64 v[14:15], v[12:13], 0, v[208:209]
	v_mov_b32_e32 v211, v3
	s_waitcnt lgkmcnt(1)
	global_store_dwordx4 v[14:15], v[4:7], off
	v_mov_b32_e32 v213, v3
	v_lshl_add_u64 v[14:15], v[12:13], 0, v[212:213]
	v_lshl_add_u64 v[4:5], v[12:13], 0, v[210:211]
	s_waitcnt lgkmcnt(0)
	global_store_dwordx4 v[4:5], v[8:11], off
	v_add_u32_e32 v4, v2, v235
	ds_read_b128 v[4:7], v4 offset:51200
	v_add_u32_e32 v2, v2, v236
	ds_read_b128 v[8:11], v2 offset:51200
	v_mov_b32_e32 v215, v3
	s_lshl_b32 s2, s18, 2
	s_waitcnt lgkmcnt(1)
	global_store_dwordx4 v[14:15], v[4:7], off
	s_add_i32 s2, s2, 7
	v_cvt_f32_ubyte0_e32 v2, s2
	v_lshl_add_u64 v[4:5], v[12:13], 0, v[214:215]
	s_waitcnt lgkmcnt(0)
	global_store_dwordx4 v[4:5], v[8:11], off
	s_waitcnt lgkmcnt(0)
	s_setprio 0
	s_barrier
	v_fmac_f32_e32 v1, 0x3ce1b529, v2
	s_mov_b64 s[4:5], 0

.LBB0_904:
	s_or_b64 exec, exec, s[74:75]
	s_waitcnt lgkmcnt(0)
	s_barrier
	ds_read_b32 v2, v237
	s_mov_b64 s[4:5], -1
	s_waitcnt lgkmcnt(0)
	v_readfirstlane_b32 s2, v2
	s_cmp_lt_i32 s2, 0
	s_cbranch_scc1 .LBB0_872
	v_readfirstlane_b32 s98, v0
	s_nop 3
	s_lshr_b32 s98, s98, 6
	s_cmp_ge_u32 s98, 4
	s_cbranch_scc0 .Lprio_skip
	s_setprio 1
.Lprio_skip:
	s_lshr_b32 s3, s2, 5
	s_and_b32 s3, s3, 6
	s_bfe_u32 s4, s2, 0x10002
	s_or_b32 s3, s3, s4
	s_bfe_u32 s6, s2, 0x30003
	s_xor_b32 s18, s6, 7
	s_lshr_b32 s22, s2, 8
	s_bfe_u32 s74, s2, 0x10001
	s_and_b32 s2, s2, 1
	s_lshl_b32 s3, s3, 1
	v_readfirstlane_b32 s75, v0
	s_or_b32 s7, s3, s74
	s_or_b32 s12, s3, s2
	s_lshr_b32 s19, s75, 6
	s_lshl_b64 s[2:3], s[22:23], 11
	s_lshl_b32 s10, s18, 8
	s_or_b32 s2, s2, s10
	s_lshl_b32 s11, s19, 5
	s_add_u32 s4, s2, s11
	s_addc_u32 s5, s3, 0
	s_lshl_b64 s[2:3], s[4:5], 11
	s_add_u32 s2, s48, s2
	s_addc_u32 s3, s49, s3
	s_lshl_b32 s7, s7, 7
	s_add_u32 s8, s2, s7
	s_addc_u32 s9, s3, 0
	s_lshl_b64 s[2:3], s[22:23], 22
	s_add_u32 s13, s84, s2
	s_addc_u32 s15, s85, s3
	s_add_u32 s14, s13, s7
	s_addc_u32 s15, s15, 0
	s_add_u32 s2, s86, s2
	s_addc_u32 s3, s87, s3
	s_lshl_b32 s7, s12, 7
	s_add_u32 s16, s2, s7
	v_mov_b32_e32 v217, v3
	s_addc_u32 s17, s3, 0
	v_lshl_add_u64 v[4:5], s[14:15], 0, v[216:217]
	s_lshl_b32 s22, s19, 4
	s_lshr_b32 s3, s75, 2
	s_and_b32 s2, s75, 0x3fffffc0
	v_lshl_add_u64 v[220:221], v[4:5], 0, s[22:23]
	v_and_or_b32 v2, s3, 48, v227
	s_and_b32 s22, s3, 0x3fffffc0
	s_lshl_b32 s76, s19, 10
	v_lshlrev_b32_e32 v2, 11, v2
	s_cmp_lg_u32 0, -1
	v_lshl_add_u64 v[4:5], s[16:17], 0, v[2:3]
	s_cselect_b32 s3, 0, 0
	v_lshl_add_u64 v[4:5], v[4:5], 0, s[22:23]
	v_mov_b32_e32 v219, v3
	s_add_i32 s76, s76, s3
	s_mov_b32 s3, m0
	s_mov_b32 m0, s76
	s_nop 0
	global_load_lds_dwordx4 v[220:221], off
	s_mov_b32 m0, s3
	v_lshl_add_u64 v[222:223], v[4:5], 0, v[218:219]
	s_add_i32 s77, s76, 0x6000
	s_mov_b32 s3, m0
	s_mov_b32 m0, s77
	s_nop 0
	global_load_lds_dwordx4 v[222:223], off
	s_mov_b32 m0, s3
	v_lshl_add_u64 v[4:5], v[220:221], 0, s[62:63]
	s_add_i32 s3, s76, 0x2000
	s_mov_b32 s7, m0
	s_mov_b32 m0, s3
	s_nop 0
	global_load_lds_dwordx4 v[4:5], off
	s_mov_b32 m0, s7
	global_load_dwordx4 v[158:161], v238, s[8:9]
	global_load_dwordx4 v[150:153], v238, s[8:9] offset:32
	global_load_dwordx4 v[142:145], v238, s[8:9] offset:64
	global_load_dwordx4 v[138:141], v238, s[8:9] offset:96
	v_mov_b32_e32 v16, v3
	v_mov_b32_e32 v17, v3
	v_mov_b32_e32 v4, v3
	v_mov_b32_e32 v5, v3
	v_mov_b32_e32 v6, v3
	v_mov_b32_e32 v7, v3
	v_mov_b32_e32 v8, v3
	v_mov_b32_e32 v9, v3
	v_mov_b32_e32 v10, v3
	v_mov_b32_e32 v11, v3
	v_mov_b32_e32 v12, v3
	v_mov_b32_e32 v13, v3
	v_mov_b32_e32 v14, v3
	v_mov_b32_e32 v15, v3
	v_mov_b32_e32 v2, v3
	v_mov_b64_e32 v[32:33], v[16:17]
	v_mov_b64_e32 v[30:31], v[14:15]
	v_mov_b64_e32 v[28:29], v[12:13]
	v_mov_b64_e32 v[26:27], v[10:11]
	v_mov_b64_e32 v[24:25], v[8:9]
	v_mov_b64_e32 v[22:23], v[6:7]
	v_mov_b64_e32 v[20:21], v[4:5]
	v_mov_b64_e32 v[18:19], v[2:3]
	v_lshl_add_u64 v[34:35], v[220:221], 0, s[64:65]
	s_add_i32 s3, s76, 0x4000
	s_mov_b32 s7, m0
	s_mov_b32 m0, s3
	s_nop 0
	global_load_lds_dwordx4 v[34:35], off
	s_mov_b32 m0, s7
	s_waitcnt vmcnt(3) lgkmcnt(0)
	s_barrier
	ds_read_b128 v[50:53], v228
	ds_read_b128 v[54:57], v228 offset:512
	s_add_i32 s7, s10, 0x100
	s_lshl_b32 s2, s2, 2
	s_add_i32 s22, s2, 0
	s_lshr_b32 s2, s7, 6
	s_mov_b32 s8, 1
	s_mov_b32 s13, 0
	s_movk_i32 s3, 0x2000
	s_movk_i32 s40, 0x4000
	v_lshl_add_u32 v207, v226, 2, s22
	s_waitcnt vmcnt(3) lgkmcnt(1)
	v_mfma_f32_32x32x16_bf16 v[34:49], v[50:53], v[158:161], v[18:33]
	s_waitcnt lgkmcnt(0)
	v_mfma_f32_32x32x16_bf16 v[18:33], v[54:57], v[158:161], v[18:33]
	ds_read_b128 v[50:53], v228 offset:2048
	ds_read_b128 v[54:57], v228 offset:2560
	s_waitcnt vmcnt(2) lgkmcnt(1)
	v_mfma_f32_32x32x16_bf16 v[34:49], v[50:53], v[150:153], v[34:49]
	s_waitcnt lgkmcnt(0)
	v_mfma_f32_32x32x16_bf16 v[18:33], v[54:57], v[150:153], v[18:33]
	ds_read_b128 v[50:53], v228 offset:4096
	ds_read_b128 v[54:57], v228 offset:4608
	s_waitcnt vmcnt(1) lgkmcnt(1)
	v_mfma_f32_32x32x16_bf16 v[34:49], v[50:53], v[142:145], v[34:49]
	s_waitcnt lgkmcnt(0)
	v_mfma_f32_32x32x16_bf16 v[18:33], v[54:57], v[142:145], v[18:33]
	ds_read_b128 v[50:53], v228 offset:6144
	ds_read_b128 v[54:57], v228 offset:6656
	s_waitcnt vmcnt(0) lgkmcnt(1)
	v_mfma_f32_32x32x16_bf16 v[34:49], v[50:53], v[138:141], v[34:49]
	s_waitcnt lgkmcnt(0)
	v_mfma_f32_32x32x16_bf16 v[18:33], v[54:57], v[138:141], v[18:33]
	s_nop 15
	s_nop 7
	s_nop 0
	v_max3_f32 v50, v34, v35, v18
	v_max3_f32 v51, v36, v37, v19
	s_nop 0
	v_max3_f32 v50, v50, v20, v21
	v_max3_f32 v51, v51, v40, v41
	s_nop 0
	v_max3_f32 v50, v50, v38, v39
	v_max3_f32 v51, v51, v24, v25
	s_nop 0
	v_max3_f32 v50, v50, v22, v23
	v_max3_f32 v51, v51, v44, v45
	s_nop 0
	v_max3_f32 v50, v50, v42, v43
	v_max3_f32 v51, v51, v28, v29
	s_nop 0
	v_max3_f32 v50, v50, v26, v27
	v_max3_f32 v51, v51, v48, v49
	s_nop 0
	v_max3_f32 v50, v50, v46, v47
	v_max3_f32 v51, v51, v32, v33
	s_nop 0
	v_max3_f32 v50, v50, v30, v31
	s_nop 0
	v_max_f32_e32 v50, v50, v51
	s_nop 0
	v_mov_b32_e32 v51, v50
	s_nop 1
	v_permlane32_swap_b32_e32 v50, v51
	v_max_f32_e32 v50, v50, v51
	s_nop 0
	v_add_f32_e32 v209, v3, v50
	v_sub_f32_e32 v34, v34, v50
	v_sub_f32_e32 v18, v18, v50
	v_sub_f32_e32 v35, v35, v50
	v_sub_f32_e32 v19, v19, v50
	v_sub_f32_e32 v36, v36, v50
	v_sub_f32_e32 v20, v20, v50
	v_sub_f32_e32 v37, v37, v50
	v_sub_f32_e32 v21, v21, v50
	v_sub_f32_e32 v38, v38, v50
	v_sub_f32_e32 v22, v22, v50
	v_sub_f32_e32 v39, v39, v50
	v_sub_f32_e32 v23, v23, v50
	v_sub_f32_e32 v40, v40, v50
	v_sub_f32_e32 v24, v24, v50
	v_sub_f32_e32 v41, v41, v50
	v_sub_f32_e32 v25, v25, v50
	v_sub_f32_e32 v42, v42, v50
	v_sub_f32_e32 v26, v26, v50
	v_sub_f32_e32 v43, v43, v50
	v_sub_f32_e32 v27, v27, v50
	v_sub_f32_e32 v44, v44, v50
	v_sub_f32_e32 v28, v28, v50
	v_sub_f32_e32 v45, v45, v50
	v_sub_f32_e32 v29, v29, v50
	v_sub_f32_e32 v46, v46, v50
	v_sub_f32_e32 v30, v30, v50
	v_sub_f32_e32 v47, v47, v50
	v_sub_f32_e32 v31, v31, v50
	v_sub_f32_e32 v48, v48, v50
	v_sub_f32_e32 v32, v32, v50
	v_sub_f32_e32 v49, v49, v50
	v_sub_f32_e32 v33, v33, v50
	s_nop 0
	v_xor_b32_e32 v50, 0x80000000, v209
	v_mov_b32_e32 v51, v50
	v_mov_b32_e32 v52, v50
	v_mov_b32_e32 v53, v50
	v_mov_b32_e32 v54, v50
	v_mov_b32_e32 v55, v50
	v_mov_b32_e32 v56, v50
	v_mov_b32_e32 v57, v50
	v_mov_b32_e32 v58, v50
	v_mov_b32_e32 v59, v50
	v_mov_b32_e32 v60, v50
	v_mov_b32_e32 v61, v50
	v_mov_b32_e32 v62, v50
	v_mov_b32_e32 v63, v50
	v_mov_b32_e32 v64, v50
	v_mov_b32_e32 v65, v50
	s_waitcnt vmcnt(0) lgkmcnt(0)
	s_barrier
	v_exp_f32_e32 v66, v18
	v_exp_f32_e32 v67, v19
	v_lshl_add_u64 v[18:19], v[220:221], 0, s[66:67]
	s_mov_b32 s7, m0
	s_mov_b32 m0, s76
	s_nop 0
	global_load_lds_dwordx4 v[18:19], off
	s_mov_b32 m0, s7
	v_lshl_add_u64 v[18:19], v[222:223], 0, s[62:63]
	s_add_i32 s7, s76, 0x8000
	s_mov_b32 s9, m0
	s_mov_b32 m0, s7
	s_nop 0
	global_load_lds_dwordx4 v[18:19], off
	s_mov_b32 m0, s9
	ds_read_b128 v[190:193], v228 offset:8192
	ds_read_b128 v[186:189], v228 offset:8704
	ds_read_b128 v[182:185], v228 offset:10240
	ds_read_b128 v[178:181], v228 offset:10752
	ds_read_b128 v[174:177], v228 offset:12288
	ds_read_b128 v[170:173], v228 offset:12800
	ds_read_b128 v[166:169], v228 offset:14336
	ds_read_b128 v[162:165], v228 offset:14848
	v_exp_f32_e32 v82, v34
	v_exp_f32_e32 v83, v35
	v_exp_f32_e32 v84, v36
	v_exp_f32_e32 v85, v37
	v_exp_f32_e32 v86, v38
	v_exp_f32_e32 v87, v39
	v_exp_f32_e32 v88, v40
	v_exp_f32_e32 v89, v41
	v_exp_f32_e32 v90, v42
	v_exp_f32_e32 v91, v43
	v_exp_f32_e32 v92, v44
	v_exp_f32_e32 v93, v45
	v_exp_f32_e32 v94, v46
	v_exp_f32_e32 v95, v47
	v_exp_f32_e32 v96, v48
	v_exp_f32_e32 v97, v49
	v_exp_f32_e32 v68, v20
	v_exp_f32_e32 v69, v21
	v_exp_f32_e32 v70, v22
	v_exp_f32_e32 v71, v23
	v_exp_f32_e32 v72, v24
	v_exp_f32_e32 v73, v25
	v_exp_f32_e32 v74, v26
	v_exp_f32_e32 v75, v27
	v_exp_f32_e32 v76, v28
	v_exp_f32_e32 v77, v29
	v_exp_f32_e32 v78, v30
	v_exp_f32_e32 v79, v31
	v_exp_f32_e32 v80, v32
	v_exp_f32_e32 v81, v33
	s_waitcnt vmcnt(2) lgkmcnt(0)
	s_barrier
	s_cmp_eq_u32 s6, 7
	s_cbranch_scc1 .LBB0_921
	v_mov_b32_e32 v16, v3
	v_mov_b32_e32 v17, v3
	v_mov_b32_e32 v2, v3
	v_mov_b32_e32 v4, v3
	v_mov_b32_e32 v5, v3
	v_mov_b32_e32 v6, v3
	v_mov_b32_e32 v7, v3
	v_mov_b32_e32 v8, v3
	v_mov_b32_e32 v9, v3
	v_mov_b32_e32 v10, v3
	v_mov_b32_e32 v11, v3
	v_mov_b32_e32 v12, v3
	v_mov_b32_e32 v13, v3
	v_mov_b32_e32 v14, v3
	v_mov_b32_e32 v15, v3
	v_mov_b64_e32 v[48:49], v[16:17]
	v_mov_b64_e32 v[32:33], v[16:17]
	v_lshl_add_u64 v[198:199], v[222:223], 0, s[66:67]
	v_lshl_add_u64 v[200:201], v[220:221], 0, s[68:69]
	s_mov_b32 s6, 0
	s_movk_i32 s13, 0x4000
	s_movk_i32 s15, 0x2000
	v_mov_b32_e32 v211, 0
	s_mov_b32 s14, 6
	v_mov_b64_e32 v[46:47], v[14:15]
	v_mov_b64_e32 v[44:45], v[12:13]
	v_mov_b64_e32 v[42:43], v[10:11]
	v_mov_b64_e32 v[40:41], v[8:9]
	v_mov_b64_e32 v[38:39], v[6:7]
	v_mov_b64_e32 v[36:37], v[4:5]
	v_mov_b64_e32 v[34:35], v[2:3]
	v_mov_b64_e32 v[30:31], v[14:15]
	v_mov_b64_e32 v[28:29], v[12:13]
	v_mov_b64_e32 v[26:27], v[10:11]
	v_mov_b64_e32 v[24:25], v[8:9]
	v_mov_b64_e32 v[22:23], v[6:7]
	v_mov_b64_e32 v[20:21], v[4:5]
	v_mov_b64_e32 v[18:19], v[2:3]
